# baseline (speedup 1.0000x reference)
.LBB3_9:
	v_lshl_add_u64 v[186:187], v[164:165], 0, s[2:3]
	v_lshl_add_u64 v[228:229], v[186:187], 0, s[12:13]
	v_lshl_add_u64 v[228:229], v[228:229], 0, s[62:63]
	s_add_i32 m0, s36, s65
	s_nop 0
	global_load_lds_dwordx4 v[228:229], off nt
	v_lshl_add_u64 v[188:189], v[178:179], 0, s[2:3]
	v_lshl_add_u64 v[228:229], v[188:189], 0, s[12:13]
	v_lshl_add_u64 v[228:229], v[228:229], 0, s[62:63]
	s_add_i32 m0, s30, s65
	s_nop 0
	global_load_lds_dwordx4 v[228:229], off nt
	v_lshl_add_u64 v[190:191], v[176:177], 0, s[2:3]
	v_lshl_add_u64 v[228:229], v[190:191], 0, s[12:13]
	v_lshl_add_u64 v[228:229], v[228:229], 0, s[62:63]
	s_add_i32 m0, s31, s65
	s_nop 0
	global_load_lds_dwordx4 v[228:229], off nt
	v_lshl_add_u64 v[192:193], v[174:175], 0, s[2:3]
	v_lshl_add_u64 v[228:229], v[192:193], 0, s[12:13]
	v_lshl_add_u64 v[228:229], v[228:229], 0, s[62:63]
	s_add_i32 m0, s40, s65
	s_nop 0
	global_load_lds_dwordx4 v[228:229], off nt
	v_add_u32_e32 v138, s48, v207
	ds_read_b64_tr_b16 v[156:157], v138 offset:24576
	ds_read_b64_tr_b16 v[158:159], v138 offset:25088
	v_add_f32_e32 v120, v80, v81
	s_waitcnt lgkmcnt(3)
	v_mfma_scale_f32_32x32x64_f8f6f4 v[48:63], v[112:119], v[96:103], v[48:63], v219, v220 op_sel_hi:[0,0,0]
	v_add_f32_e32 v112, v82, v120
	v_add_f32_e32 v112, v83, v112
	v_add_f32_e32 v112, v84, v112
	v_add_f32_e32 v116, v85, v112
	v_cvt_pk_f16_f32 v132, v80, v81
	v_cvt_pk_f16_f32 v133, v82, v83
	ds_read_b64_tr_b16 v[112:113], v138 offset:28672
	ds_read_b64_tr_b16 v[114:115], v138 offset:29184
	v_add_f32_e32 v80, v86, v116
	v_add_f32_e32 v80, v87, v80
	v_add_f32_e32 v80, v88, v80
	v_add_f32_e32 v80, v89, v80
	v_cvt_pk_f16_f32 v134, v84, v85
	v_cvt_pk_f16_f32 v135, v86, v87
	s_waitcnt lgkmcnt(4)
	v_mfma_scale_f32_32x32x64_f8f6f4 v[32:47], v[104:111], v[96:103], v[32:47], v219, v220 op_sel_hi:[0,0,0]
	ds_read_b64_tr_b16 v[104:105], v138 offset:25600
	ds_read_b64_tr_b16 v[106:107], v138 offset:26112
	v_add_f32_e32 v80, v90, v80
	v_add_f32_e32 v80, v91, v80
	v_add_f32_e32 v80, v92, v80
	v_add_f32_e32 v80, v93, v80
	v_cvt_pk_f16_f32 v128, v88, v89
	v_cvt_pk_f16_f32 v129, v90, v91
	ds_read_b64_tr_b16 v[152:153], v138 offset:29696
	ds_read_b64_tr_b16 v[154:155], v138 offset:30208
	v_add_f32_e32 v80, v94, v80
	v_add_f32_e32 v80, v95, v80
	v_add_f32_e32 v80, v64, v80
	v_add_f32_e32 v80, v65, v80
	v_cvt_pk_f16_f32 v130, v92, v93
	v_cvt_pk_f16_f32 v131, v94, v95
	ds_read_b64_tr_b16 v[148:149], v138 offset:26624
	ds_read_b64_tr_b16 v[150:151], v138 offset:27136
	v_add_f32_e32 v80, v66, v80
	v_add_f32_e32 v80, v67, v80
	v_add_f32_e32 v80, v68, v80
	v_add_f32_e32 v80, v69, v80
	v_cvt_pk_f16_f32 v124, v64, v65
	v_cvt_pk_f16_f32 v125, v66, v67
	ds_read_b64_tr_b16 v[144:145], v138 offset:30720
	ds_read_b64_tr_b16 v[146:147], v138 offset:31232
	v_add_f32_e32 v64, v70, v80
	v_add_f32_e32 v64, v71, v64
	v_add_f32_e32 v64, v72, v64
	v_add_f32_e32 v64, v73, v64
	v_cvt_pk_f16_f32 v126, v68, v69
	v_cvt_pk_f16_f32 v127, v70, v71
	ds_read_b64_tr_b16 v[140:141], v138 offset:27648
	ds_read_b64_tr_b16 v[142:143], v138 offset:28160
	v_add_f32_e32 v64, v74, v64
	v_add_f32_e32 v64, v75, v64
	v_add_f32_e32 v64, v76, v64
	v_add_f32_e32 v64, v77, v64
	v_cvt_pk_f16_f32 v120, v72, v73
	v_cvt_pk_f16_f32 v121, v74, v75
	ds_read_b64_tr_b16 v[136:137], v138 offset:31744
	ds_read_b64_tr_b16 v[138:139], v138 offset:32256
	v_add_f32_e32 v64, v78, v64
	v_add_f32_e32 v64, v79, v64
	v_add_f32_e32 v108, 0, v64
	v_cvt_pk_f16_f32 v122, v76, v77
	v_cvt_pk_f16_f32 v123, v78, v79
	s_nop 1
	s_nop 0
	v_add_f32_e32 v185, v185, v108
	v_max_f32_e32 v108, v49, v49
	v_max_f32_e32 v109, v48, v48
	v_max_f32_e32 v108, v109, v108
	v_max3_f32 v109, v50, v51, v33
	v_max3_f32 v108, v108, v32, v34
	v_max3_f32 v108, v108, v35, v52
	v_max3_f32 v109, v109, v54, v55
	v_max3_f32 v108, v108, v53, v36
	v_max3_f32 v109, v109, v38, v39
	v_max3_f32 v108, v108, v37, v56
	v_max3_f32 v109, v109, v58, v59
	v_add_u32_e32 v221, v222, v223
	v_max3_f32 v108, v108, v57, v40
	v_max3_f32 v109, v109, v42, v43
	ds_read_b128 v[80:83], v221
	ds_read_b128 v[64:67], v161
	ds_read_b128 v[84:87], v184
	ds_read_b128 v[68:71], v211
	ds_read_b128 v[88:91], v212
	ds_read_b128 v[72:75], v213
	ds_read_b128 v[92:95], v214
	ds_read_b128 v[76:79], v215
	v_max3_f32 v108, v108, v41, v60
	v_max3_f32 v109, v109, v62, v63
	v_max3_f32 v108, v108, v61, v44
	v_max3_f32 v109, v109, v46, v47
	v_max3_f32 v108, v108, v45, v109
	v_mov_b32_e32 v109, v108
	s_nop 1
	v_permlane32_swap_b32_e32 v108, v109
	v_max_f32_e32 v109, v109, v109
	v_max_f32_e32 v108, v108, v108
	v_max_f32_e32 v108, v108, v109
	v_fma_f32 v108, v108, s39, -v208
	v_cmp_lt_f32_e32 vcc, s46, v108
	s_cmp_lg_u64 vcc, 0
	s_cselect_b64 s[26:27], -1, 0
	s_cbranch_vccnz .LBB3_21

.LBB3_14:
	v_lshl_add_u64 v[228:229], v[186:187], 0, s[22:23]
	v_lshl_add_u64 v[228:229], v[228:229], 0, s[62:63]
	s_add_i32 m0, s36, s64
	s_nop 0
	global_load_lds_dwordx4 v[228:229], off nt
	v_lshl_add_u64 v[228:229], v[188:189], 0, s[22:23]
	v_lshl_add_u64 v[228:229], v[228:229], 0, s[62:63]
	s_add_i32 m0, s30, s64
	s_nop 0
	global_load_lds_dwordx4 v[228:229], off nt
	v_lshl_add_u64 v[228:229], v[190:191], 0, s[22:23]
	v_lshl_add_u64 v[228:229], v[228:229], 0, s[62:63]
	s_add_i32 m0, s31, s64
	s_nop 0
	global_load_lds_dwordx4 v[228:229], off nt
	v_lshl_add_u64 v[228:229], v[192:193], 0, s[22:23]
	v_lshl_add_u64 v[228:229], v[228:229], 0, s[62:63]
	s_add_i32 m0, s40, s64
	s_nop 0
	global_load_lds_dwordx4 v[228:229], off nt
	v_add_u32_e32 v138, s47, v207
	ds_read_b64_tr_b16 v[156:157], v138 offset:24576
	ds_read_b64_tr_b16 v[158:159], v138 offset:25088
	v_add_f32_e32 v120, v48, v49
	s_waitcnt lgkmcnt(4)
	v_mfma_scale_f32_32x32x64_f8f6f4 v[80:95], v[112:119], v[96:103], v[80:95], v219, v220 op_sel_hi:[0,0,0]
	v_add_f32_e32 v112, v50, v120
	v_add_f32_e32 v112, v51, v112
	v_add_f32_e32 v112, v52, v112
	v_add_f32_e32 v116, v53, v112
	v_cvt_pk_f16_f32 v132, v48, v49
	v_cvt_pk_f16_f32 v133, v50, v51
	ds_read_b64_tr_b16 v[112:113], v138 offset:28672
	ds_read_b64_tr_b16 v[114:115], v138 offset:29184
	v_add_f32_e32 v48, v54, v116
	v_add_f32_e32 v48, v55, v48
	v_add_f32_e32 v48, v56, v48
	v_add_f32_e32 v48, v57, v48
	v_cvt_pk_f16_f32 v134, v52, v53
	v_cvt_pk_f16_f32 v135, v54, v55
	s_waitcnt lgkmcnt(4)
	v_mfma_scale_f32_32x32x64_f8f6f4 v[64:79], v[104:111], v[96:103], v[64:79], v219, v220 op_sel_hi:[0,0,0]
	ds_read_b64_tr_b16 v[104:105], v138 offset:25600
	ds_read_b64_tr_b16 v[106:107], v138 offset:26112
	v_add_f32_e32 v48, v58, v48
	v_add_f32_e32 v48, v59, v48
	v_add_f32_e32 v48, v60, v48
	v_add_f32_e32 v48, v61, v48
	v_cvt_pk_f16_f32 v128, v56, v57
	v_cvt_pk_f16_f32 v129, v58, v59
	ds_read_b64_tr_b16 v[152:153], v138 offset:29696
	ds_read_b64_tr_b16 v[154:155], v138 offset:30208
	v_add_f32_e32 v48, v62, v48
	v_add_f32_e32 v48, v63, v48
	v_add_f32_e32 v48, v32, v48
	v_add_f32_e32 v48, v33, v48
	v_cvt_pk_f16_f32 v130, v60, v61
	v_cvt_pk_f16_f32 v131, v62, v63
	ds_read_b64_tr_b16 v[148:149], v138 offset:26624
	ds_read_b64_tr_b16 v[150:151], v138 offset:27136
	v_add_f32_e32 v48, v34, v48
	v_add_f32_e32 v48, v35, v48
	v_add_f32_e32 v48, v36, v48
	v_add_f32_e32 v48, v37, v48
	v_cvt_pk_f16_f32 v124, v32, v33
	v_cvt_pk_f16_f32 v125, v34, v35
	ds_read_b64_tr_b16 v[144:145], v138 offset:30720
	ds_read_b64_tr_b16 v[146:147], v138 offset:31232
	v_add_f32_e32 v32, v38, v48
	v_add_f32_e32 v32, v39, v32
	v_add_f32_e32 v32, v40, v32
	v_add_f32_e32 v32, v41, v32
	v_cvt_pk_f16_f32 v126, v36, v37
	v_cvt_pk_f16_f32 v127, v38, v39
	ds_read_b64_tr_b16 v[140:141], v138 offset:27648
	ds_read_b64_tr_b16 v[142:143], v138 offset:28160
	v_add_f32_e32 v32, v42, v32
	v_add_f32_e32 v32, v43, v32
	v_add_f32_e32 v32, v44, v32
	v_add_f32_e32 v32, v45, v32
	v_cvt_pk_f16_f32 v120, v40, v41
	v_cvt_pk_f16_f32 v121, v42, v43
	ds_read_b64_tr_b16 v[136:137], v138 offset:31744
	ds_read_b64_tr_b16 v[138:139], v138 offset:32256
	v_add_f32_e32 v32, v46, v32
	v_add_f32_e32 v32, v47, v32
	v_add_f32_e32 v108, 0, v32
	v_cvt_pk_f16_f32 v122, v44, v45
	v_cvt_pk_f16_f32 v123, v46, v47
	s_nop 1
	s_nop 0
	v_add_f32_e32 v185, v185, v108
	v_max_f32_e32 v108, v81, v81
	v_max_f32_e32 v109, v80, v80
	v_max_f32_e32 v108, v109, v108
	v_max3_f32 v109, v82, v83, v65
	v_max3_f32 v108, v108, v64, v66
	v_max3_f32 v108, v108, v67, v84
	v_max3_f32 v109, v109, v86, v87
	v_max3_f32 v108, v108, v85, v68
	v_max3_f32 v109, v109, v70, v71
	v_max3_f32 v108, v108, v69, v88
	v_max3_f32 v109, v109, v90, v91
	v_max3_f32 v108, v108, v89, v72
	v_max3_f32 v109, v109, v74, v75
	ds_read_b128 v[48:51], v221 offset:32768
	ds_read_b128 v[32:35], v161 offset:32768
	ds_read_b128 v[52:55], v184 offset:32768
	ds_read_b128 v[36:39], v211 offset:32768
	ds_read_b128 v[56:59], v212 offset:32768
	ds_read_b128 v[40:43], v213 offset:32768
	ds_read_b128 v[60:63], v214 offset:32768
	ds_read_b128 v[44:47], v215 offset:32768
	v_max3_f32 v108, v108, v73, v92
	v_max3_f32 v109, v109, v94, v95
	v_max3_f32 v108, v108, v93, v76
	v_max3_f32 v109, v109, v78, v79
	v_max3_f32 v108, v108, v77, v109
	v_mov_b32_e32 v109, v108
	s_nop 1
	v_permlane32_swap_b32_e32 v108, v109
	v_max_f32_e32 v109, v109, v109
	v_max_f32_e32 v108, v108, v108
	v_max_f32_e32 v108, v108, v109
	v_fma_f32 v108, v108, s39, -v208
	v_cmp_lt_f32_e32 vcc, s46, v108
	s_cmp_lg_u64 vcc, 0
	s_cselect_b64 s[26:27], -1, 0
	s_cbranch_vccnz .LBB3_24

.LBB6_9:
	v_lshl_add_u64 v[186:187], v[164:165], 0, s[2:3]
	v_lshl_add_u64 v[228:229], v[186:187], 0, s[10:11]
	v_lshl_add_u64 v[228:229], v[228:229], 0, s[62:63]
	s_add_i32 m0, s38, s65
	s_nop 0
	global_load_lds_dwordx4 v[228:229], off nt
	v_lshl_add_u64 v[188:189], v[178:179], 0, s[2:3]
	v_lshl_add_u64 v[228:229], v[188:189], 0, s[10:11]
	v_lshl_add_u64 v[228:229], v[228:229], 0, s[62:63]
	s_add_i32 m0, s30, s65
	s_nop 0
	global_load_lds_dwordx4 v[228:229], off nt
	v_lshl_add_u64 v[190:191], v[176:177], 0, s[2:3]
	v_lshl_add_u64 v[228:229], v[190:191], 0, s[10:11]
	v_lshl_add_u64 v[228:229], v[228:229], 0, s[62:63]
	s_add_i32 m0, s31, s65
	s_nop 0
	global_load_lds_dwordx4 v[228:229], off nt
	v_lshl_add_u64 v[192:193], v[174:175], 0, s[2:3]
	v_lshl_add_u64 v[228:229], v[192:193], 0, s[10:11]
	v_lshl_add_u64 v[228:229], v[228:229], 0, s[62:63]
	s_add_i32 m0, s34, s65
	s_nop 0
	global_load_lds_dwordx4 v[228:229], off nt
	v_add_u32_e32 v138, s27, v207
	ds_read_b64_tr_b16 v[156:157], v138 offset:24576
	ds_read_b64_tr_b16 v[158:159], v138 offset:25088
	v_add_f32_e32 v120, v80, v81
	s_waitcnt lgkmcnt(3)
	v_mfma_scale_f32_32x32x64_f8f6f4 v[48:63], v[112:119], v[96:103], v[48:63], v219, v220 op_sel_hi:[0,0,0]
	v_add_f32_e32 v112, v82, v120
	v_add_f32_e32 v112, v83, v112
	v_add_f32_e32 v112, v84, v112
	v_add_f32_e32 v116, v85, v112
	v_cvt_pk_f16_f32 v132, v80, v81
	v_cvt_pk_f16_f32 v133, v82, v83
	ds_read_b64_tr_b16 v[112:113], v138 offset:28672
	ds_read_b64_tr_b16 v[114:115], v138 offset:29184
	v_add_f32_e32 v80, v86, v116
	v_add_f32_e32 v80, v87, v80
	v_add_f32_e32 v80, v88, v80
	v_add_f32_e32 v80, v89, v80
	v_cvt_pk_f16_f32 v134, v84, v85
	v_cvt_pk_f16_f32 v135, v86, v87
	s_waitcnt lgkmcnt(4)
	v_mfma_scale_f32_32x32x64_f8f6f4 v[32:47], v[104:111], v[96:103], v[32:47], v219, v220 op_sel_hi:[0,0,0]
	ds_read_b64_tr_b16 v[104:105], v138 offset:25600
	ds_read_b64_tr_b16 v[106:107], v138 offset:26112
	v_add_f32_e32 v80, v90, v80
	v_add_f32_e32 v80, v91, v80
	v_add_f32_e32 v80, v92, v80
	v_add_f32_e32 v80, v93, v80
	v_cvt_pk_f16_f32 v128, v88, v89
	v_cvt_pk_f16_f32 v129, v90, v91
	ds_read_b64_tr_b16 v[152:153], v138 offset:29696
	ds_read_b64_tr_b16 v[154:155], v138 offset:30208
	v_add_f32_e32 v80, v94, v80
	v_add_f32_e32 v80, v95, v80
	v_add_f32_e32 v80, v64, v80
	v_add_f32_e32 v80, v65, v80
	v_cvt_pk_f16_f32 v130, v92, v93
	v_cvt_pk_f16_f32 v131, v94, v95
	ds_read_b64_tr_b16 v[148:149], v138 offset:26624
	ds_read_b64_tr_b16 v[150:151], v138 offset:27136
	v_add_f32_e32 v80, v66, v80
	v_add_f32_e32 v80, v67, v80
	v_add_f32_e32 v80, v68, v80
	v_add_f32_e32 v80, v69, v80
	v_cvt_pk_f16_f32 v124, v64, v65
	v_cvt_pk_f16_f32 v125, v66, v67
	ds_read_b64_tr_b16 v[144:145], v138 offset:30720
	ds_read_b64_tr_b16 v[146:147], v138 offset:31232
	v_add_f32_e32 v64, v70, v80
	v_add_f32_e32 v64, v71, v64
	v_add_f32_e32 v64, v72, v64
	v_add_f32_e32 v64, v73, v64
	v_cvt_pk_f16_f32 v126, v68, v69
	v_cvt_pk_f16_f32 v127, v70, v71
	ds_read_b64_tr_b16 v[140:141], v138 offset:27648
	ds_read_b64_tr_b16 v[142:143], v138 offset:28160
	v_add_f32_e32 v64, v74, v64
	v_add_f32_e32 v64, v75, v64
	v_add_f32_e32 v64, v76, v64
	v_add_f32_e32 v64, v77, v64
	v_cvt_pk_f16_f32 v120, v72, v73
	v_cvt_pk_f16_f32 v121, v74, v75
	ds_read_b64_tr_b16 v[136:137], v138 offset:31744
	ds_read_b64_tr_b16 v[138:139], v138 offset:32256
	v_add_f32_e32 v64, v78, v64
	v_add_f32_e32 v64, v79, v64
	v_add_f32_e32 v108, 0, v64
	v_cvt_pk_f16_f32 v122, v76, v77
	v_cvt_pk_f16_f32 v123, v78, v79
	s_nop 1
	s_nop 0
	v_add_f32_e32 v185, v185, v108
	v_max_f32_e32 v108, v49, v49
	v_max_f32_e32 v109, v48, v48
	v_max_f32_e32 v108, v109, v108
	v_max3_f32 v109, v50, v51, v33
	v_max3_f32 v108, v108, v32, v34
	v_max3_f32 v108, v108, v35, v52
	v_max3_f32 v109, v109, v54, v55
	v_max3_f32 v108, v108, v53, v36
	v_max3_f32 v109, v109, v38, v39
	v_max3_f32 v108, v108, v37, v56
	v_max3_f32 v109, v109, v58, v59
	v_add_u32_e32 v221, v222, v223
	v_max3_f32 v108, v108, v57, v40
	v_max3_f32 v109, v109, v42, v43
	ds_read_b128 v[80:83], v221
	ds_read_b128 v[64:67], v161
	ds_read_b128 v[84:87], v184
	ds_read_b128 v[68:71], v211
	ds_read_b128 v[88:91], v212
	ds_read_b128 v[72:75], v213
	ds_read_b128 v[92:95], v214
	ds_read_b128 v[76:79], v215
	v_max3_f32 v108, v108, v41, v60
	v_max3_f32 v109, v109, v62, v63
	v_max3_f32 v108, v108, v61, v44
	v_max3_f32 v109, v109, v46, v47
	v_max3_f32 v108, v108, v45, v109
	v_mov_b32_e32 v109, v108
	s_nop 1
	v_permlane32_swap_b32_e32 v108, v109
	v_max_f32_e32 v109, v109, v109
	v_max_f32_e32 v108, v108, v108
	v_max_f32_e32 v108, v108, v109
	v_fma_f32 v108, v108, s41, -v208
	v_cmp_lt_f32_e32 vcc, s29, v108
	s_cmp_lg_u64 vcc, 0
	s_cselect_b64 s[24:25], -1, 0
	s_cbranch_vccnz .LBB6_21

.LBB6_14:
	v_lshl_add_u64 v[228:229], v[186:187], 0, s[22:23]
	v_lshl_add_u64 v[228:229], v[228:229], 0, s[62:63]
	s_add_i32 m0, s38, s64
	s_nop 0
	global_load_lds_dwordx4 v[228:229], off nt
	v_lshl_add_u64 v[228:229], v[188:189], 0, s[22:23]
	v_lshl_add_u64 v[228:229], v[228:229], 0, s[62:63]
	s_add_i32 m0, s30, s64
	s_nop 0
	global_load_lds_dwordx4 v[228:229], off nt
	v_lshl_add_u64 v[228:229], v[190:191], 0, s[22:23]
	v_lshl_add_u64 v[228:229], v[228:229], 0, s[62:63]
	s_add_i32 m0, s31, s64
	s_nop 0
	global_load_lds_dwordx4 v[228:229], off nt
	v_lshl_add_u64 v[228:229], v[192:193], 0, s[22:23]
	v_lshl_add_u64 v[228:229], v[228:229], 0, s[62:63]
	s_add_i32 m0, s34, s64
	s_nop 0
	global_load_lds_dwordx4 v[228:229], off nt
	v_add_u32_e32 v138, s45, v207
	ds_read_b64_tr_b16 v[156:157], v138 offset:24576
	ds_read_b64_tr_b16 v[158:159], v138 offset:25088
	v_add_f32_e32 v120, v48, v49
	s_waitcnt lgkmcnt(4)
	v_mfma_scale_f32_32x32x64_f8f6f4 v[80:95], v[112:119], v[96:103], v[80:95], v219, v220 op_sel_hi:[0,0,0]
	v_add_f32_e32 v112, v50, v120
	v_add_f32_e32 v112, v51, v112
	v_add_f32_e32 v112, v52, v112
	v_add_f32_e32 v116, v53, v112
	v_cvt_pk_f16_f32 v132, v48, v49
	v_cvt_pk_f16_f32 v133, v50, v51
	ds_read_b64_tr_b16 v[112:113], v138 offset:28672
	ds_read_b64_tr_b16 v[114:115], v138 offset:29184
	v_add_f32_e32 v48, v54, v116
	v_add_f32_e32 v48, v55, v48
	v_add_f32_e32 v48, v56, v48
	v_add_f32_e32 v48, v57, v48
	v_cvt_pk_f16_f32 v134, v52, v53
	v_cvt_pk_f16_f32 v135, v54, v55
	s_waitcnt lgkmcnt(4)
	v_mfma_scale_f32_32x32x64_f8f6f4 v[64:79], v[104:111], v[96:103], v[64:79], v219, v220 op_sel_hi:[0,0,0]
	ds_read_b64_tr_b16 v[104:105], v138 offset:25600
	ds_read_b64_tr_b16 v[106:107], v138 offset:26112
	v_add_f32_e32 v48, v58, v48
	v_add_f32_e32 v48, v59, v48
	v_add_f32_e32 v48, v60, v48
	v_add_f32_e32 v48, v61, v48
	v_cvt_pk_f16_f32 v128, v56, v57
	v_cvt_pk_f16_f32 v129, v58, v59
	ds_read_b64_tr_b16 v[152:153], v138 offset:29696
	ds_read_b64_tr_b16 v[154:155], v138 offset:30208
	v_add_f32_e32 v48, v62, v48
	v_add_f32_e32 v48, v63, v48
	v_add_f32_e32 v48, v32, v48
	v_add_f32_e32 v48, v33, v48
	v_cvt_pk_f16_f32 v130, v60, v61
	v_cvt_pk_f16_f32 v131, v62, v63
	ds_read_b64_tr_b16 v[148:149], v138 offset:26624
	ds_read_b64_tr_b16 v[150:151], v138 offset:27136
	v_add_f32_e32 v48, v34, v48
	v_add_f32_e32 v48, v35, v48
	v_add_f32_e32 v48, v36, v48
	v_add_f32_e32 v48, v37, v48
	v_cvt_pk_f16_f32 v124, v32, v33
	v_cvt_pk_f16_f32 v125, v34, v35
	ds_read_b64_tr_b16 v[144:145], v138 offset:30720
	ds_read_b64_tr_b16 v[146:147], v138 offset:31232
	v_add_f32_e32 v32, v38, v48
	v_add_f32_e32 v32, v39, v32
	v_add_f32_e32 v32, v40, v32
	v_add_f32_e32 v32, v41, v32
	v_cvt_pk_f16_f32 v126, v36, v37
	v_cvt_pk_f16_f32 v127, v38, v39
	ds_read_b64_tr_b16 v[140:141], v138 offset:27648
	ds_read_b64_tr_b16 v[142:143], v138 offset:28160
	v_add_f32_e32 v32, v42, v32
	v_add_f32_e32 v32, v43, v32
	v_add_f32_e32 v32, v44, v32
	v_add_f32_e32 v32, v45, v32
	v_cvt_pk_f16_f32 v120, v40, v41
	v_cvt_pk_f16_f32 v121, v42, v43
	ds_read_b64_tr_b16 v[136:137], v138 offset:31744
	ds_read_b64_tr_b16 v[138:139], v138 offset:32256
	v_add_f32_e32 v32, v46, v32
	v_add_f32_e32 v32, v47, v32
	v_add_f32_e32 v108, 0, v32
	v_cvt_pk_f16_f32 v122, v44, v45
	v_cvt_pk_f16_f32 v123, v46, v47
	s_nop 1
	s_nop 0
	v_add_f32_e32 v185, v185, v108
	v_max_f32_e32 v108, v81, v81
	v_max_f32_e32 v109, v80, v80
	v_max_f32_e32 v108, v109, v108
	v_max3_f32 v109, v82, v83, v65
	v_max3_f32 v108, v108, v64, v66
	v_max3_f32 v108, v108, v67, v84
	v_max3_f32 v109, v109, v86, v87
	v_max3_f32 v108, v108, v85, v68
	v_max3_f32 v109, v109, v70, v71
	v_max3_f32 v108, v108, v69, v88
	v_max3_f32 v109, v109, v90, v91
	v_max3_f32 v108, v108, v89, v72
	v_max3_f32 v109, v109, v74, v75
	ds_read_b128 v[48:51], v221 offset:32768
	ds_read_b128 v[32:35], v161 offset:32768
	ds_read_b128 v[52:55], v184 offset:32768
	ds_read_b128 v[36:39], v211 offset:32768
	ds_read_b128 v[56:59], v212 offset:32768
	ds_read_b128 v[40:43], v213 offset:32768
	ds_read_b128 v[60:63], v214 offset:32768
	ds_read_b128 v[44:47], v215 offset:32768
	v_max3_f32 v108, v108, v73, v92
	v_max3_f32 v109, v109, v94, v95
	v_max3_f32 v108, v108, v93, v76
	v_max3_f32 v109, v109, v78, v79
	v_max3_f32 v108, v108, v77, v109
	v_mov_b32_e32 v109, v108
	s_nop 1
	v_permlane32_swap_b32_e32 v108, v109
	v_max_f32_e32 v109, v109, v109
	v_max_f32_e32 v108, v108, v108
	v_max_f32_e32 v108, v108, v109
	v_fma_f32 v108, v108, s41, -v208
	v_cmp_lt_f32_e32 vcc, s29, v108
	s_cmp_lg_u64 vcc, 0
	s_cselect_b64 s[24:25], -1, 0
	s_cbranch_vccnz .LBB6_24
